# post-projection per-token loop: all 18 loads of a token issued in one burst at the top (one global round trip per token)
# speedup vs baseline: 1.0018x; 1.0016x over previous
.LBB0_324:
	s_or_b64 exec, exec, s[72:73]
	v_lshl_add_u64 v[36:37], s[50:51], 0, v[22:23]
	v_add_co_u32_e32 v38, vcc, 0x37cd0000, v36
	v_mov_b32_e32 v45, 0
	s_nop 0
	v_addc_co_u32_e32 v39, vcc, 0, v37, vcc
	v_lshl_add_u64 v[40:41], s[50:51], 0, v[10:11]
	v_add_co_u32_e32 v40, vcc, 0x4d6d0000, v40
	v_lshl_add_u64 v[42:43], s[50:51], 0, v[20:21]
	s_nop 0
	v_addc_co_u32_e32 v41, vcc, 0, v41, vcc
	v_add_co_u32_e32 v36, vcc, s15, v36
	v_mov_b32_e32 v46, 0
	s_nop 0
	v_addc_co_u32_e32 v37, vcc, 0, v37, vcc
	v_mov_b32_e32 v47, 0
	v_mov_b32_e32 v48, 0
	v_mov_b32_e32 v49, 0
	v_mov_b32_e32 v50, 0
	s_add_i32 s14, s14, s16
	s_add_u32 s0, s0, s18
	s_addc_u32 s1, s1, s19
	v_lshl_add_u64 v[6:7], v[6:7], 0, s[20:21]
	v_lshl_add_u64 v[10:11], v[10:11], 0, s[20:21]
	v_lshl_add_u64 v[16:17], v[16:17], 0, s[52:53]
	v_lshl_add_u64 v[20:21], v[20:21], 0, s[52:53]
	v_lshl_add_u64 v[22:23], v[22:23], 0, s[52:53]
	v_lshl_add_u64 v[24:25], v[24:25], 0, s[52:53]
	s_cmpk_gt_i32 s14, 0x3fff
	v_lshl_add_u64 v[26:27], v[26:27], 0, s[52:53]
	s_waitcnt vmcnt(10)
	v_lshlrev_b32_e32 v44, 16, v238
	v_cvt_pk_fp8_f32 v45, v44, v44
	v_mov_b32_e32 v44, 0
	global_store_byte v[40:41], v45, off offset:32
	v_mov_b32_e32 v45, 0
	v_lshlrev_b32_e32 v42, 16, v239
	v_cvt_pk_fp8_f32 v44, v42, v42
	v_lshl_add_u64 v[42:43], s[50:51], 0, v[12:13]
	v_lshl_add_u64 v[12:13], v[12:13], 0, s[20:21]
	global_store_byte v[42:43], v44, off
	v_mov_b32_e32 v42, 0
	v_lshlrev_b32_e32 v38, 16, v240
	v_cvt_pk_fp8_f32 v42, v38, v38
	v_lshl_add_u64 v[38:39], s[50:51], 0, v[18:19]
	v_lshl_add_u64 v[18:19], v[18:19], 0, s[52:53]
	global_store_byte v[40:41], v42, off offset:192
	s_nop 0
	v_lshl_add_u64 v[36:37], s[50:51], 0, v[8:9]
	v_lshl_add_u64 v[40:41], s[50:51], 0, v[14:15]
	v_lshl_add_u64 v[8:9], v[8:9], 0, s[20:21]
	v_lshl_add_u64 v[14:15], v[14:15], 0, s[26:27]
	v_lshlrev_b32_e32 v42, 16, v241
	v_lshlrev_b32_e32 v51, 16, v246
	v_and_b32_e32 v38, 0xffff0000, v246
	v_cvt_pk_fp8_f32 v45, v51, v38
	s_nop 0
	v_add_f32_dpp v38, v42, v42 row_shr:1 row_mask:0xf bank_mask:0xf bound_ctrl:1
	s_nop 1
	v_add_f32_dpp v38, v38, v38 row_shr:2 row_mask:0xf bank_mask:0xf bound_ctrl:1
	s_nop 1
	v_add_f32_dpp v38, v38, v38 row_shr:4 row_mask:0xf bank_mask:0xf bound_ctrl:1
	s_nop 1
	v_add_f32_dpp v38, v38, v38 row_shr:8 row_mask:0xf bank_mask:0xf bound_ctrl:1
	s_nop 1
	v_mov_b32_dpp v46, v38 row_bcast:15 row_mask:0xa bank_mask:0xf
	v_add_f32_e32 v38, v38, v46
	s_nop 1
	v_mov_b32_dpp v47, v38 row_bcast:31 row_mask:0xc bank_mask:0xf
	v_add_f32_e32 v38, v38, v47
	s_nop 0
	v_readlane_b32 s29, v38, 63
	s_nop 1
	v_fmac_f32_e32 v42, s29, v32
	v_mul_f32_e32 v38, v42, v42
	s_nop 1
	v_mov_b32_dpp v48, v38 row_shr:1 row_mask:0xf bank_mask:0xf
	v_fmac_f32_e32 v48, v42, v42
	s_nop 1
	v_add_f32_dpp v38, v48, v48 row_shr:2 row_mask:0xf bank_mask:0xf bound_ctrl:1
	s_nop 1
	v_add_f32_dpp v38, v38, v38 row_shr:4 row_mask:0xf bank_mask:0xf bound_ctrl:1
	s_nop 1
	v_add_f32_dpp v38, v38, v38 row_shr:8 row_mask:0xf bank_mask:0xf bound_ctrl:1
	s_nop 1
	v_mov_b32_dpp v49, v38 row_bcast:15 row_mask:0xa bank_mask:0xf
	v_add_f32_e32 v38, v38, v49
	s_nop 1
	v_mov_b32_dpp v50, v38 row_bcast:31 row_mask:0xc bank_mask:0xf
	v_add_f32_e32 v38, v38, v50
	s_nop 0
	v_readlane_b32 s29, v38, 63
	s_nop 1
	v_fma_f32 v38, s29, v33, v31
	v_mul_f32_e32 v46, 0x4b800000, v38
	v_cmp_gt_f32_e32 vcc, s17, v38
	s_nop 1
	v_cndmask_b32_e32 v38, v38, v46, vcc
	v_rsq_f32_e32 v38, v38
	v_lshlrev_b32_e32 v46, 16, v247
	v_and_b32_e32 v39, 0xffff0000, v247
	v_cvt_pk_fp8_f32 v45, v46, v39 op_sel:[0,0,1]
	v_mul_f32_e32 v39, 0x45800000, v38
	v_cndmask_b32_e32 v38, v38, v39, vcc
	v_mul_f32_e32 v38, v42, v38
	v_fma_f32 v44, v248, v38, v249
	ds_bpermute_b32 v38, v29, v44
	v_mul_f32_e32 v35, v35, v44
	global_store_dword v[36:37], v45, off
	s_waitcnt lgkmcnt(0)
	v_fma_f32 v36, -v34, v38, v35
	v_fmac_f32_e32 v35, v34, v38
	v_cndmask_b32_e64 v34, v44, v35, s[10:11]
	v_cndmask_b32_e64 v34, v34, v36, s[8:9]
	v_bfe_u32 v35, v34, 16, 1
	v_add3_u32 v34, v34, v35, s3
	global_store_short_d16_hi v[40:41], v34, off
	s_cbranch_scc1 .LBB0_327
.LBB0_325:
	global_load_dword v36, v195, s[0:1]
	v_lshl_add_u64 v[34:35], s[50:51], 0, v[26:27]
	global_load_ushort v37, v[34:35], off offset:-1024
	global_load_ushort v40, v[34:35], off offset:-992
	global_load_ushort v42, v[34:35], off
	global_load_ushort v43, v[34:35], off offset:32
	v_lshl_add_u64 v[38:39], s[50:51], 0, v[24:25]
	global_load_ushort v250, v[38:39], off offset:-1024
	global_load_ushort v251, v[38:39], off offset:-1008
	global_load_ushort v252, v[38:39], off
	global_load_ushort v253, v[38:39], off offset:16
	s_mov_b32 s98, 0x37cd0000
	s_mov_b32 s99, 0
	v_lshl_add_u64 v[244:245], s[50:51], 0, v[16:17]
	v_lshl_add_u64 v[244:245], v[244:245], 0, s[98:99]
	s_mov_b64 s[96:97], exec
	s_and_b64 exec, exec, s[6:7]
	global_load_ushort v254, v[244:245], off offset:2048
	global_load_ushort v255, v[244:245], off offset:2080
	s_mov_b64 exec, s[96:97]
	s_mov_b32 s96, s15
	s_mov_b32 s97, 0
	v_lshl_add_u64 v[242:243], s[50:51], 0, v[22:23]
	v_lshl_add_u64 v[242:243], v[242:243], 0, s[98:99]
	global_load_ushort v238, v[242:243], off offset:2112
	global_load_ushort v240, v[242:243], off offset:2432
	v_lshl_add_u64 v[242:243], s[50:51], 0, v[20:21]
	global_load_ushort v239, v[242:243], off
	v_lshl_add_u64 v[242:243], s[50:51], 0, v[18:19]
	global_load_dwordx2 v[246:247], v[242:243], off
	v_lshl_add_u64 v[242:243], s[50:51], 0, v[22:23]
	v_lshl_add_u64 v[242:243], v[242:243], 0, s[96:97]
	global_load_ushort v241, v[242:243], off offset:1024
	global_load_dword v248, v[2:3], off
	global_load_dword v249, v[4:5], off
	s_waitcnt vmcnt(16)
	v_lshlrev_b32_e32 v45, 16, v37
	v_cvt_f32_i32_e32 v44, v36
	s_waitcnt vmcnt(15)
	v_lshlrev_b32_e32 v46, 16, v40
	v_mul_f32_e32 v36, v1, v44
	v_cvt_f64_f32_e32 v[36:37], v36
	v_mul_f64 v[40:41], v[36:37], s[62:63]
	v_rndne_f64_e32 v[40:41], v[40:41]
	v_fmac_f64_e32 v[36:37], s[70:71], v[40:41]
	v_cvt_f32_f64_e32 v36, v[36:37]
	v_mul_f32_e32 v37, 0.15915494, v36
	v_sin_f32_e32 v36, v37
	v_cos_f32_e32 v37, v37
	s_waitcnt vmcnt(14)
	v_lshlrev_b32_e32 v40, 16, v42
	s_waitcnt vmcnt(13)
	v_lshlrev_b32_e32 v41, 16, v43
	v_mul_f32_e32 v42, v36, v46
	v_mul_f32_e32 v43, v37, v46
	v_mul_f32_e32 v46, v36, v41
	v_mul_f32_e32 v41, v37, v41
	v_fma_f32 v42, v37, v45, -v42
	v_fmac_f32_e32 v43, v36, v45
	v_fma_f32 v45, v37, v40, -v46
	v_fmac_f32_e32 v41, v36, v40
	v_bfe_u32 v40, v42, 16, 1
	v_bfe_u32 v46, v43, 16, 1
	v_bfe_u32 v47, v45, 16, 1
	v_bfe_u32 v48, v41, 16, 1
	v_add3_u32 v40, v42, v40, s3
	v_add3_u32 v42, v43, v46, s3
	v_add3_u32 v43, v45, v47, s3
	v_add3_u32 v41, v41, v48, s3
	global_store_short_d16_hi v[34:35], v40, off offset:-1024
	global_store_short_d16_hi v[34:35], v42, off offset:-992
	global_store_short_d16_hi v[34:35], v43, off
	global_store_short_d16_hi v[34:35], v41, off offset:32
	s_nop 0
	v_mul_f32_e32 v34, v28, v44
	v_cvt_f64_f32_e32 v[34:35], v34
	v_mul_f64 v[40:41], v[34:35], s[62:63]
	v_rndne_f64_e32 v[40:41], v[40:41]
	v_fmac_f64_e32 v[34:35], s[70:71], v[40:41]
	v_cvt_f32_f64_e32 v34, v[34:35]
	v_mul_f32_e32 v35, 0.15915494, v34
	v_sin_f32_e32 v34, v35
	v_cos_f32_e32 v35, v35
	s_waitcnt vmcnt(13)
	v_lshlrev_b32_e32 v40, 16, v250
	v_lshlrev_b32_e32 v41, 16, v251
	v_mul_f32_e32 v44, v34, v41
	v_lshlrev_b32_e32 v43, 16, v253
	v_lshlrev_b32_e32 v42, 16, v252
	v_mul_f32_e32 v41, v35, v41
	v_mul_f32_e32 v45, v34, v43
	v_mul_f32_e32 v43, v35, v43
	v_fma_f32 v44, v35, v40, -v44
	v_fmac_f32_e32 v41, v34, v40
	v_fma_f32 v40, v35, v42, -v45
	v_fmac_f32_e32 v43, v34, v42
	v_bfe_u32 v42, v44, 16, 1
	v_bfe_u32 v45, v41, 16, 1
	v_bfe_u32 v46, v40, 16, 1
	v_bfe_u32 v47, v43, 16, 1
	v_add3_u32 v42, v44, v42, s3
	v_add3_u32 v41, v41, v45, s3
	v_add3_u32 v40, v40, v46, s3
	v_add3_u32 v43, v43, v47, s3
	global_store_short_d16_hi v[38:39], v42, off offset:-1024
	global_store_short_d16_hi v[38:39], v41, off offset:-1008
	global_store_short_d16_hi v[38:39], v40, off
	global_store_short_d16_hi v[38:39], v43, off offset:16
	s_and_saveexec_b64 s[72:73], s[6:7]
	s_cbranch_execz .LBB0_324
	v_lshl_add_u64 v[38:39], s[50:51], 0, v[16:17]
	v_add_co_u32_e32 v38, vcc, 0x37cd0000, v38
	v_mov_b32_e32 v42, 0
	s_nop 0
	v_addc_co_u32_e32 v39, vcc, 0, v39, vcc
	v_mov_b32_e32 v43, 0
	v_lshl_add_u64 v[38:39], s[50:51], 0, v[6:7]
	v_add_co_u32_e32 v38, vcc, 0x4d6d0000, v38
	s_waitcnt vmcnt(15)
	v_lshlrev_b32_e32 v40, 16, v254
	v_lshlrev_b32_e32 v41, 16, v255
	v_mul_f32_e32 v44, v36, v41
	v_mul_f32_e32 v41, v37, v41
	v_fma_f32 v37, v37, v40, -v44
	v_fmac_f32_e32 v41, v36, v40
	v_cvt_pk_fp8_f32 v42, v37, v37
	v_cvt_pk_fp8_f32 v43, v41, v41
	v_addc_co_u32_e32 v39, vcc, 0, v39, vcc
	global_store_byte v[38:39], v42, off
	global_store_byte v[38:39], v43, off offset:16
	s_branch .LBB0_324
